# v2
# speedup vs baseline: 1.0104x; 1.0010x over previous
.LBB0_9:
	s_waitcnt vmcnt(15)
	v_cvt_pk_bf16_f32 v2, v34, v35
	v_cvt_pk_bf16_f32 v3, v36, v37
	s_waitcnt vmcnt(11)
	v_cvt_pk_bf16_f32 v10, v50, v51
	v_cvt_pk_bf16_f32 v11, v52, v53
	v_cvt_pk_bf16_f32 v4, v38, v39
	v_cvt_pk_bf16_f32 v5, v40, v41
	ds_write2_b64 v212, v[2:3], v[10:11] offset1:68
	s_waitcnt vmcnt(10)
	v_cvt_pk_bf16_f32 v2, v54, v55
	v_cvt_pk_bf16_f32 v3, v56, v57
	v_cvt_pk_bf16_f32 v6, v42, v43
	v_cvt_pk_bf16_f32 v7, v44, v45
	ds_write2_b64 v215, v[4:5], v[2:3] offset0:16 offset1:84
	s_waitcnt vmcnt(9)
	v_cvt_pk_bf16_f32 v2, v58, v59
	v_cvt_pk_bf16_f32 v3, v60, v61
	v_cvt_pk_bf16_f32 v8, v46, v47
	v_cvt_pk_bf16_f32 v9, v48, v49
	ds_write2_b64 v216, v[6:7], v[2:3] offset0:32 offset1:100
	s_waitcnt vmcnt(8)
	v_cvt_pk_bf16_f32 v2, v62, v63
	v_cvt_pk_bf16_f32 v3, v64, v65
	ds_write2_b64 v217, v[8:9], v[2:3] offset0:48 offset1:116
	s_waitcnt vmcnt(7)
	v_cvt_pk_bf16_f32 v2, v66, v67
	v_cvt_pk_bf16_f32 v3, v68, v69
	s_waitcnt vmcnt(3)
	v_cvt_pk_bf16_f32 v10, v82, v83
	v_cvt_pk_bf16_f32 v11, v84, v85
	v_cvt_pk_bf16_f32 v4, v70, v71
	v_cvt_pk_bf16_f32 v5, v72, v73
	ds_write2_b64 v212, v[2:3], v[10:11] offset0:136 offset1:204
	s_waitcnt vmcnt(2)
	v_cvt_pk_bf16_f32 v2, v86, v87
	v_cvt_pk_bf16_f32 v3, v88, v89
	v_cvt_pk_bf16_f32 v6, v74, v75
	v_cvt_pk_bf16_f32 v7, v76, v77
	ds_write2_b64 v215, v[4:5], v[2:3] offset0:152 offset1:220
	s_waitcnt vmcnt(1)
	v_cvt_pk_bf16_f32 v2, v90, v91
	v_cvt_pk_bf16_f32 v3, v92, v93
	v_cvt_pk_bf16_f32 v8, v78, v79
	v_cvt_pk_bf16_f32 v9, v80, v81
	ds_write2_b64 v216, v[6:7], v[2:3] offset0:168 offset1:236
	s_waitcnt vmcnt(0)
	v_cvt_pk_bf16_f32 v2, v94, v95
	v_cvt_pk_bf16_f32 v3, v96, v97
	ds_write2_b64 v217, v[8:9], v[2:3] offset0:184 offset1:252
	s_add_i32 s26, s35, 8
	s_cmpk_lt_i32 s26, 0x80
	s_mov_b64 s[24:25], -1
	s_cbranch_scc1 .LBB0_15
	global_load_dwordx4 v[26:29], v[134:135], off offset:16
	global_load_dwordx4 v[30:33], v[134:135], off
	global_load_dwordx4 v[18:21], v[134:135], off offset:144
	global_load_dwordx4 v[22:25], v[134:135], off offset:128
	global_load_dwordx4 v[10:13], v[134:135], off offset:272
	global_load_dwordx4 v[14:17], v[134:135], off offset:256
	global_load_dwordx4 v[2:5], v[134:135], off offset:400
	global_load_dwordx4 v[6:9], v[134:135], off offset:384
	s_mov_b64 s[24:25], 0

.LBB0_17:
	s_waitcnt lgkmcnt(0)
	s_ashr_i32 s27, s35, 5
	s_cmp_eq_u32 s27, s34
	s_cbranch_scc1 .LBB0_37
	ds_bpermute_b32 v98, v208, v218
	v_max_f32_e32 v99, v218, v218
	v_mov_b32_e32 v101, 0
	v_mov_b32_e32 v102, 0
	v_mov_b32_e32 v103, 0
	s_waitcnt lgkmcnt(0)
	v_max_f32_e32 v98, v98, v98
	v_max_f32_e32 v98, v99, v98
	ds_bpermute_b32 v99, v207, v98
	v_mov_b32_e32 v104, 0
	v_mov_b32_e32 v105, 0
	v_mov_b32_e32 v106, 0
	s_lshl_b32 s24, s34, 3
	s_waitcnt lgkmcnt(0)
	v_max_f32_e32 v99, v99, v99
	v_max_f32_e32 v98, v98, v99
	ds_bpermute_b32 v100, v206, v98
	s_add_i32 s24, s24, s31
	s_mul_i32 s28, s24, 0x210
	v_mov_b32_e32 v99, 0
	s_add_i32 s28, s28, 0x23440
	s_waitcnt lgkmcnt(0)
	v_max_f32_e32 v100, v100, v100
	v_max_f32_e32 v98, v98, v100
	ds_bpermute_b32 v100, v205, v98
	v_add_u32_e32 v111, s28, v203
	s_waitcnt lgkmcnt(0)
	v_max_f32_e32 v100, v100, v100
	v_max_f32_e32 v98, v98, v100
	v_sub_f32_e32 v100, v218, v98
	v_exp_f32_e32 v100, v100
	s_nop 0
	v_mul_f32_e32 v107, v219, v100
	v_pk_mul_f32 v[108:109], v[100:101], v[198:199] op_sel_hi:[0,1]
	s_nop 0
	v_mov_b32_dpp v101, v107 row_shr:1 row_mask:0xf bank_mask:0xf
	v_fmac_f32_e32 v101, v219, v100
	v_mov_b32_dpp v102, v108 row_shr:1 row_mask:0xf bank_mask:0xf
	v_mov_b32_dpp v103, v109 row_shr:1 row_mask:0xf bank_mask:0xf
	v_pk_fma_f32 v[102:103], v[100:101], v[198:199], v[102:103] op_sel_hi:[0,1,1]
	v_mov_b32_e32 v107, 0
	v_add_f32_dpp v101, v101, v101 row_shr:2 row_mask:0xf bank_mask:0xf bound_ctrl:1
	v_mov_b32_dpp v104, v102 row_shr:2 row_mask:0xf bank_mask:0xf
	v_mov_b32_dpp v105, v103 row_shr:2 row_mask:0xf bank_mask:0xf
	v_pk_add_f32 v[102:103], v[102:103], v[104:105]
	v_mov_b32_e32 v108, 0
	v_mov_b32_e32 v109, 0
	v_mov_b32_dpp v106, v102 row_shr:4 row_mask:0xf bank_mask:0xf
	v_mov_b32_dpp v107, v103 row_shr:4 row_mask:0xf bank_mask:0xf
	v_pk_add_f32 v[102:103], v[102:103], v[106:107]
	v_pk_mul_f32 v[106:107], v[100:101], v[196:197] op_sel_hi:[0,1]
	v_add_f32_dpp v110, v101, v101 row_shr:4 row_mask:0xf bank_mask:0xf bound_ctrl:1
	v_mov_b32_e32 v104, 0
	v_mov_b32_dpp v108, v106 row_shr:1 row_mask:0xf bank_mask:0xf
	v_mov_b32_dpp v109, v107 row_shr:1 row_mask:0xf bank_mask:0xf
	v_pk_fma_f32 v[106:107], v[100:101], v[196:197], v[108:109] op_sel_hi:[0,1,1]
	v_mov_b32_e32 v108, 0
	v_mov_b32_e32 v109, 0
	v_mov_b32_e32 v105, 0
	v_mov_b32_dpp v108, v106 row_shr:2 row_mask:0xf bank_mask:0xf
	v_mov_b32_dpp v109, v107 row_shr:2 row_mask:0xf bank_mask:0xf
	v_pk_add_f32 v[106:107], v[106:107], v[108:109]
	v_mov_b32_e32 v108, 0
	v_mov_b32_e32 v109, 0
	v_mov_b32_dpp v99, v110 row_shr:8 row_mask:0xf bank_mask:0xf
	v_mov_b32_dpp v108, v106 row_shr:4 row_mask:0xf bank_mask:0xf
	v_mov_b32_dpp v109, v107 row_shr:4 row_mask:0xf bank_mask:0xf
	v_pk_add_f32 v[106:107], v[106:107], v[108:109]
	v_mov_b32_e32 v108, 0
	v_mov_b32_e32 v109, 0
	v_mov_b32_dpp v104, v102 row_shr:8 row_mask:0xf bank_mask:0xf
	v_mov_b32_dpp v105, v103 row_shr:8 row_mask:0xf bank_mask:0xf
	v_mov_b32_dpp v108, v106 row_shr:8 row_mask:0xf bank_mask:0xf
	v_mov_b32_dpp v109, v107 row_shr:8 row_mask:0xf bank_mask:0xf
	s_and_saveexec_b64 s[24:25], s[6:7]
	v_pk_add_f32 v[106:107], v[106:107], v[108:109]
	v_pk_add_f32 v[104:105], v[102:103], v[104:105]
	ds_write_b128 v111, v[104:107]
	s_or_b64 exec, exec, s[24:25]
	v_mov_b32_e32 v101, v100
	v_pk_mul_f32 v[102:103], v[100:101], v[194:195]
	v_mov_b32_e32 v104, 0
	v_mov_b32_e32 v105, 0
	v_pk_mul_f32 v[106:107], v[100:101], v[192:193]
	v_mov_b32_e32 v108, 0
	v_mov_b32_e32 v109, 0
	v_mov_b32_dpp v104, v102 row_shr:1 row_mask:0xf bank_mask:0xf
	v_mov_b32_dpp v105, v103 row_shr:1 row_mask:0xf bank_mask:0xf
	v_mov_b32_dpp v108, v106 row_shr:1 row_mask:0xf bank_mask:0xf
	v_mov_b32_dpp v109, v107 row_shr:1 row_mask:0xf bank_mask:0xf
	v_pk_fma_f32 v[102:103], v[100:101], v[194:195], v[104:105]
	v_mov_b32_e32 v104, 0
	v_mov_b32_e32 v105, 0
	v_pk_fma_f32 v[106:107], v[100:101], v[192:193], v[108:109]
	v_mov_b32_e32 v108, 0
	v_mov_b32_e32 v109, 0
	v_mov_b32_dpp v104, v102 row_shr:2 row_mask:0xf bank_mask:0xf
	v_mov_b32_dpp v105, v103 row_shr:2 row_mask:0xf bank_mask:0xf
	v_mov_b32_dpp v108, v106 row_shr:2 row_mask:0xf bank_mask:0xf
	v_mov_b32_dpp v109, v107 row_shr:2 row_mask:0xf bank_mask:0xf
	v_pk_add_f32 v[102:103], v[102:103], v[104:105]
	v_mov_b32_e32 v104, 0
	v_mov_b32_e32 v105, 0
	v_pk_add_f32 v[106:107], v[106:107], v[108:109]
	v_mov_b32_e32 v108, 0
	v_mov_b32_e32 v109, 0
	v_mov_b32_dpp v104, v102 row_shr:4 row_mask:0xf bank_mask:0xf
	v_mov_b32_dpp v105, v103 row_shr:4 row_mask:0xf bank_mask:0xf
	v_mov_b32_dpp v108, v106 row_shr:4 row_mask:0xf bank_mask:0xf
	v_mov_b32_dpp v109, v107 row_shr:4 row_mask:0xf bank_mask:0xf
	v_pk_add_f32 v[102:103], v[102:103], v[104:105]
	v_mov_b32_e32 v104, 0
	v_mov_b32_e32 v105, 0
	v_pk_add_f32 v[106:107], v[106:107], v[108:109]
	v_mov_b32_e32 v108, 0
	v_mov_b32_e32 v109, 0
	v_mov_b32_dpp v104, v102 row_shr:8 row_mask:0xf bank_mask:0xf
	v_mov_b32_dpp v105, v103 row_shr:8 row_mask:0xf bank_mask:0xf
	v_mov_b32_dpp v108, v106 row_shr:8 row_mask:0xf bank_mask:0xf
	v_mov_b32_dpp v109, v107 row_shr:8 row_mask:0xf bank_mask:0xf
	s_and_saveexec_b64 s[24:25], s[6:7]
	v_pk_add_f32 v[106:107], v[106:107], v[108:109]
	v_pk_add_f32 v[104:105], v[102:103], v[104:105]
	ds_write_b128 v111, v[104:107] offset:64
	s_or_b64 exec, exec, s[24:25]
	v_pk_mul_f32 v[102:103], v[100:101], v[190:191]
	v_mov_b32_e32 v104, 0
	v_mov_b32_e32 v105, 0
	v_pk_mul_f32 v[106:107], v[100:101], v[188:189]
	v_mov_b32_e32 v108, 0
	v_mov_b32_e32 v109, 0
	v_mov_b32_dpp v104, v102 row_shr:1 row_mask:0xf bank_mask:0xf
	v_mov_b32_dpp v105, v103 row_shr:1 row_mask:0xf bank_mask:0xf
	v_mov_b32_dpp v108, v106 row_shr:1 row_mask:0xf bank_mask:0xf
	v_mov_b32_dpp v109, v107 row_shr:1 row_mask:0xf bank_mask:0xf
	v_pk_fma_f32 v[102:103], v[100:101], v[190:191], v[104:105]
	v_mov_b32_e32 v104, 0
	v_mov_b32_e32 v105, 0
	v_pk_fma_f32 v[106:107], v[100:101], v[188:189], v[108:109]
	v_mov_b32_e32 v108, 0
	v_mov_b32_e32 v109, 0
	v_mov_b32_dpp v104, v102 row_shr:2 row_mask:0xf bank_mask:0xf
	v_mov_b32_dpp v105, v103 row_shr:2 row_mask:0xf bank_mask:0xf
	v_mov_b32_dpp v108, v106 row_shr:2 row_mask:0xf bank_mask:0xf
	v_mov_b32_dpp v109, v107 row_shr:2 row_mask:0xf bank_mask:0xf
	v_pk_add_f32 v[102:103], v[102:103], v[104:105]
	v_mov_b32_e32 v104, 0
	v_mov_b32_e32 v105, 0
	v_pk_add_f32 v[106:107], v[106:107], v[108:109]
	v_mov_b32_e32 v108, 0
	v_mov_b32_e32 v109, 0
	v_mov_b32_dpp v104, v102 row_shr:4 row_mask:0xf bank_mask:0xf
	v_mov_b32_dpp v105, v103 row_shr:4 row_mask:0xf bank_mask:0xf
	v_mov_b32_dpp v108, v106 row_shr:4 row_mask:0xf bank_mask:0xf
	v_mov_b32_dpp v109, v107 row_shr:4 row_mask:0xf bank_mask:0xf
	v_pk_add_f32 v[102:103], v[102:103], v[104:105]
	v_mov_b32_e32 v104, 0
	v_mov_b32_e32 v105, 0
	v_pk_add_f32 v[106:107], v[106:107], v[108:109]
	v_mov_b32_e32 v108, 0
	v_mov_b32_e32 v109, 0
	v_mov_b32_dpp v104, v102 row_shr:8 row_mask:0xf bank_mask:0xf
	v_mov_b32_dpp v105, v103 row_shr:8 row_mask:0xf bank_mask:0xf
	v_mov_b32_dpp v108, v106 row_shr:8 row_mask:0xf bank_mask:0xf
	v_mov_b32_dpp v109, v107 row_shr:8 row_mask:0xf bank_mask:0xf
	s_and_saveexec_b64 s[24:25], s[6:7]
	v_pk_add_f32 v[106:107], v[106:107], v[108:109]
	v_pk_add_f32 v[104:105], v[102:103], v[104:105]
	ds_write_b128 v111, v[104:107] offset:128
	s_or_b64 exec, exec, s[24:25]
	v_pk_mul_f32 v[102:103], v[100:101], v[186:187]
	v_mov_b32_e32 v104, 0
	v_mov_b32_e32 v105, 0
	v_pk_mul_f32 v[106:107], v[100:101], v[184:185]
	v_mov_b32_e32 v108, 0
	v_mov_b32_e32 v109, 0
	v_mov_b32_dpp v104, v102 row_shr:1 row_mask:0xf bank_mask:0xf
	v_mov_b32_dpp v105, v103 row_shr:1 row_mask:0xf bank_mask:0xf
	v_mov_b32_dpp v108, v106 row_shr:1 row_mask:0xf bank_mask:0xf
	v_mov_b32_dpp v109, v107 row_shr:1 row_mask:0xf bank_mask:0xf
	v_pk_fma_f32 v[102:103], v[100:101], v[186:187], v[104:105]
	v_mov_b32_e32 v104, 0
	v_mov_b32_e32 v105, 0
	v_pk_fma_f32 v[106:107], v[100:101], v[184:185], v[108:109]
	v_mov_b32_e32 v108, 0
	v_mov_b32_e32 v109, 0
	v_mov_b32_dpp v104, v102 row_shr:2 row_mask:0xf bank_mask:0xf
	v_mov_b32_dpp v105, v103 row_shr:2 row_mask:0xf bank_mask:0xf
	v_mov_b32_dpp v108, v106 row_shr:2 row_mask:0xf bank_mask:0xf
	v_mov_b32_dpp v109, v107 row_shr:2 row_mask:0xf bank_mask:0xf
	v_pk_add_f32 v[102:103], v[102:103], v[104:105]
	v_mov_b32_e32 v104, 0
	v_mov_b32_e32 v105, 0
	v_pk_add_f32 v[106:107], v[106:107], v[108:109]
	v_mov_b32_e32 v108, 0
	v_mov_b32_e32 v109, 0
	v_mov_b32_dpp v104, v102 row_shr:4 row_mask:0xf bank_mask:0xf
	v_mov_b32_dpp v105, v103 row_shr:4 row_mask:0xf bank_mask:0xf
	v_mov_b32_dpp v108, v106 row_shr:4 row_mask:0xf bank_mask:0xf
	v_mov_b32_dpp v109, v107 row_shr:4 row_mask:0xf bank_mask:0xf
	v_pk_add_f32 v[102:103], v[102:103], v[104:105]
	v_mov_b32_e32 v104, 0
	v_mov_b32_e32 v105, 0
	v_pk_add_f32 v[106:107], v[106:107], v[108:109]
	v_mov_b32_e32 v108, 0
	v_mov_b32_e32 v109, 0
	v_mov_b32_dpp v104, v102 row_shr:8 row_mask:0xf bank_mask:0xf
	v_mov_b32_dpp v105, v103 row_shr:8 row_mask:0xf bank_mask:0xf
	v_mov_b32_dpp v108, v106 row_shr:8 row_mask:0xf bank_mask:0xf
	v_mov_b32_dpp v109, v107 row_shr:8 row_mask:0xf bank_mask:0xf
	s_and_saveexec_b64 s[24:25], s[6:7]
	v_pk_add_f32 v[106:107], v[106:107], v[108:109]
	v_pk_add_f32 v[104:105], v[102:103], v[104:105]
	ds_write_b128 v111, v[104:107] offset:192
	s_or_b64 exec, exec, s[24:25]
	v_pk_mul_f32 v[102:103], v[100:101], v[182:183]
	v_mov_b32_e32 v104, 0
	v_mov_b32_e32 v105, 0
	v_pk_mul_f32 v[106:107], v[100:101], v[180:181]
	v_mov_b32_e32 v108, 0
	v_mov_b32_e32 v109, 0
	v_mov_b32_dpp v104, v102 row_shr:1 row_mask:0xf bank_mask:0xf
	v_mov_b32_dpp v105, v103 row_shr:1 row_mask:0xf bank_mask:0xf
	v_mov_b32_dpp v108, v106 row_shr:1 row_mask:0xf bank_mask:0xf
	v_mov_b32_dpp v109, v107 row_shr:1 row_mask:0xf bank_mask:0xf
	v_pk_fma_f32 v[102:103], v[100:101], v[182:183], v[104:105]
	v_mov_b32_e32 v104, 0
	v_mov_b32_e32 v105, 0
	v_pk_fma_f32 v[106:107], v[100:101], v[180:181], v[108:109]
	v_mov_b32_e32 v108, 0
	v_mov_b32_e32 v109, 0
	v_mov_b32_dpp v104, v102 row_shr:2 row_mask:0xf bank_mask:0xf
	v_mov_b32_dpp v105, v103 row_shr:2 row_mask:0xf bank_mask:0xf
	v_mov_b32_dpp v108, v106 row_shr:2 row_mask:0xf bank_mask:0xf
	v_mov_b32_dpp v109, v107 row_shr:2 row_mask:0xf bank_mask:0xf
	v_pk_add_f32 v[102:103], v[102:103], v[104:105]
	v_mov_b32_e32 v104, 0
	v_mov_b32_e32 v105, 0
	v_pk_add_f32 v[106:107], v[106:107], v[108:109]
	v_mov_b32_e32 v108, 0
	v_mov_b32_e32 v109, 0
	v_mov_b32_dpp v104, v102 row_shr:4 row_mask:0xf bank_mask:0xf
	v_mov_b32_dpp v105, v103 row_shr:4 row_mask:0xf bank_mask:0xf
	v_mov_b32_dpp v108, v106 row_shr:4 row_mask:0xf bank_mask:0xf
	v_mov_b32_dpp v109, v107 row_shr:4 row_mask:0xf bank_mask:0xf
	v_pk_add_f32 v[102:103], v[102:103], v[104:105]
	v_mov_b32_e32 v104, 0
	v_mov_b32_e32 v105, 0
	v_pk_add_f32 v[106:107], v[106:107], v[108:109]
	v_mov_b32_e32 v108, 0
	v_mov_b32_e32 v109, 0
	v_mov_b32_dpp v104, v102 row_shr:8 row_mask:0xf bank_mask:0xf
	v_mov_b32_dpp v105, v103 row_shr:8 row_mask:0xf bank_mask:0xf
	v_mov_b32_dpp v108, v106 row_shr:8 row_mask:0xf bank_mask:0xf
	v_mov_b32_dpp v109, v107 row_shr:8 row_mask:0xf bank_mask:0xf
	s_and_saveexec_b64 s[24:25], s[6:7]
	v_pk_add_f32 v[106:107], v[106:107], v[108:109]
	v_pk_add_f32 v[104:105], v[102:103], v[104:105]
	ds_write_b128 v111, v[104:107] offset:256
	s_or_b64 exec, exec, s[24:25]
	v_pk_mul_f32 v[102:103], v[100:101], v[178:179]
	v_mov_b32_e32 v104, 0
	v_mov_b32_e32 v105, 0
	v_pk_mul_f32 v[106:107], v[100:101], v[168:169]
	v_mov_b32_e32 v108, 0
	v_mov_b32_e32 v109, 0
	v_mov_b32_dpp v104, v102 row_shr:1 row_mask:0xf bank_mask:0xf
	v_mov_b32_dpp v105, v103 row_shr:1 row_mask:0xf bank_mask:0xf
	v_mov_b32_dpp v108, v106 row_shr:1 row_mask:0xf bank_mask:0xf
	v_mov_b32_dpp v109, v107 row_shr:1 row_mask:0xf bank_mask:0xf
	v_pk_fma_f32 v[102:103], v[100:101], v[178:179], v[104:105]
	v_mov_b32_e32 v104, 0
	v_mov_b32_e32 v105, 0
	v_pk_fma_f32 v[106:107], v[100:101], v[168:169], v[108:109]
	v_mov_b32_e32 v108, 0
	v_mov_b32_e32 v109, 0
	v_mov_b32_dpp v104, v102 row_shr:2 row_mask:0xf bank_mask:0xf
	v_mov_b32_dpp v105, v103 row_shr:2 row_mask:0xf bank_mask:0xf
	v_mov_b32_dpp v108, v106 row_shr:2 row_mask:0xf bank_mask:0xf
	v_mov_b32_dpp v109, v107 row_shr:2 row_mask:0xf bank_mask:0xf
	v_pk_add_f32 v[102:103], v[102:103], v[104:105]
	v_mov_b32_e32 v104, 0
	v_mov_b32_e32 v105, 0
	v_pk_add_f32 v[106:107], v[106:107], v[108:109]
	v_mov_b32_e32 v108, 0
	v_mov_b32_e32 v109, 0
	v_mov_b32_dpp v104, v102 row_shr:4 row_mask:0xf bank_mask:0xf
	v_mov_b32_dpp v105, v103 row_shr:4 row_mask:0xf bank_mask:0xf
	v_mov_b32_dpp v108, v106 row_shr:4 row_mask:0xf bank_mask:0xf
	v_mov_b32_dpp v109, v107 row_shr:4 row_mask:0xf bank_mask:0xf
	v_pk_add_f32 v[102:103], v[102:103], v[104:105]
	v_mov_b32_e32 v104, 0
	v_mov_b32_e32 v105, 0
	v_pk_add_f32 v[106:107], v[106:107], v[108:109]
	v_mov_b32_e32 v108, 0
	v_mov_b32_e32 v109, 0
	v_mov_b32_dpp v104, v102 row_shr:8 row_mask:0xf bank_mask:0xf
	v_mov_b32_dpp v105, v103 row_shr:8 row_mask:0xf bank_mask:0xf
	v_mov_b32_dpp v108, v106 row_shr:8 row_mask:0xf bank_mask:0xf
	v_mov_b32_dpp v109, v107 row_shr:8 row_mask:0xf bank_mask:0xf
	s_and_saveexec_b64 s[24:25], s[6:7]
	v_pk_add_f32 v[106:107], v[106:107], v[108:109]
	v_pk_add_f32 v[104:105], v[102:103], v[104:105]
	ds_write_b128 v111, v[104:107] offset:320
	s_or_b64 exec, exec, s[24:25]
	v_pk_mul_f32 v[102:103], v[100:101], v[150:151]
	v_mov_b32_e32 v104, 0
	v_mov_b32_e32 v105, 0
	v_pk_mul_f32 v[106:107], v[100:101], v[140:141]
	v_mov_b32_e32 v108, 0
	v_mov_b32_e32 v109, 0
	v_mov_b32_dpp v104, v102 row_shr:1 row_mask:0xf bank_mask:0xf
	v_mov_b32_dpp v105, v103 row_shr:1 row_mask:0xf bank_mask:0xf
	v_mov_b32_dpp v108, v106 row_shr:1 row_mask:0xf bank_mask:0xf
	v_mov_b32_dpp v109, v107 row_shr:1 row_mask:0xf bank_mask:0xf
	v_pk_fma_f32 v[102:103], v[100:101], v[150:151], v[104:105]
	v_mov_b32_e32 v104, 0
	v_mov_b32_e32 v105, 0
	v_pk_fma_f32 v[106:107], v[100:101], v[140:141], v[108:109]
	v_mov_b32_e32 v108, 0
	v_mov_b32_e32 v109, 0
	v_mov_b32_dpp v104, v102 row_shr:2 row_mask:0xf bank_mask:0xf
	v_mov_b32_dpp v105, v103 row_shr:2 row_mask:0xf bank_mask:0xf
	v_mov_b32_dpp v108, v106 row_shr:2 row_mask:0xf bank_mask:0xf
	v_mov_b32_dpp v109, v107 row_shr:2 row_mask:0xf bank_mask:0xf
	v_pk_add_f32 v[102:103], v[102:103], v[104:105]
	v_mov_b32_e32 v104, 0
	v_mov_b32_e32 v105, 0
	v_pk_add_f32 v[106:107], v[106:107], v[108:109]
	v_mov_b32_e32 v108, 0
	v_mov_b32_e32 v109, 0
	v_mov_b32_dpp v104, v102 row_shr:4 row_mask:0xf bank_mask:0xf
	v_mov_b32_dpp v105, v103 row_shr:4 row_mask:0xf bank_mask:0xf
	v_mov_b32_dpp v108, v106 row_shr:4 row_mask:0xf bank_mask:0xf
	v_mov_b32_dpp v109, v107 row_shr:4 row_mask:0xf bank_mask:0xf
	v_pk_add_f32 v[102:103], v[102:103], v[104:105]
	v_mov_b32_e32 v104, 0
	v_mov_b32_e32 v105, 0
	v_pk_add_f32 v[106:107], v[106:107], v[108:109]
	v_mov_b32_e32 v108, 0
	v_mov_b32_e32 v109, 0
	v_mov_b32_dpp v104, v102 row_shr:8 row_mask:0xf bank_mask:0xf
	v_mov_b32_dpp v105, v103 row_shr:8 row_mask:0xf bank_mask:0xf
	v_mov_b32_dpp v108, v106 row_shr:8 row_mask:0xf bank_mask:0xf
	v_mov_b32_dpp v109, v107 row_shr:8 row_mask:0xf bank_mask:0xf
	s_and_saveexec_b64 s[24:25], s[6:7]
	v_pk_add_f32 v[106:107], v[106:107], v[108:109]
	v_pk_add_f32 v[104:105], v[102:103], v[104:105]
	ds_write_b128 v111, v[104:107] offset:384
	s_or_b64 exec, exec, s[24:25]
	v_pk_mul_f32 v[102:103], v[100:101], v[138:139]
	v_mov_b32_e32 v104, 0
	v_mov_b32_e32 v105, 0
	v_pk_mul_f32 v[106:107], v[100:101], v[136:137]
	v_mov_b32_e32 v108, 0
	v_mov_b32_e32 v109, 0
	v_mov_b32_dpp v104, v102 row_shr:1 row_mask:0xf bank_mask:0xf
	v_mov_b32_dpp v105, v103 row_shr:1 row_mask:0xf bank_mask:0xf
	v_mov_b32_dpp v108, v106 row_shr:1 row_mask:0xf bank_mask:0xf
	v_mov_b32_dpp v109, v107 row_shr:1 row_mask:0xf bank_mask:0xf
	v_pk_fma_f32 v[102:103], v[100:101], v[138:139], v[104:105]
	v_mov_b32_e32 v104, 0
	v_mov_b32_e32 v105, 0
	v_pk_fma_f32 v[100:101], v[100:101], v[136:137], v[108:109]
	v_mov_b32_e32 v106, 0
	v_mov_b32_e32 v107, 0
	v_mov_b32_dpp v104, v102 row_shr:2 row_mask:0xf bank_mask:0xf
	v_mov_b32_dpp v105, v103 row_shr:2 row_mask:0xf bank_mask:0xf
	v_mov_b32_dpp v106, v100 row_shr:2 row_mask:0xf bank_mask:0xf
	v_mov_b32_dpp v107, v101 row_shr:2 row_mask:0xf bank_mask:0xf
	v_pk_add_f32 v[102:103], v[102:103], v[104:105]
	v_mov_b32_e32 v104, 0
	v_mov_b32_e32 v105, 0
	v_pk_add_f32 v[100:101], v[100:101], v[106:107]
	v_mov_b32_e32 v106, 0
	v_mov_b32_e32 v107, 0
	v_mov_b32_dpp v104, v102 row_shr:4 row_mask:0xf bank_mask:0xf
	v_mov_b32_dpp v105, v103 row_shr:4 row_mask:0xf bank_mask:0xf
	v_mov_b32_dpp v106, v100 row_shr:4 row_mask:0xf bank_mask:0xf
	v_mov_b32_dpp v107, v101 row_shr:4 row_mask:0xf bank_mask:0xf
	v_pk_add_f32 v[102:103], v[102:103], v[104:105]
	v_mov_b32_e32 v104, 0
	v_mov_b32_e32 v105, 0
	v_pk_add_f32 v[100:101], v[100:101], v[106:107]
	v_mov_b32_e32 v106, 0
	v_mov_b32_e32 v107, 0
	v_mov_b32_dpp v104, v102 row_shr:8 row_mask:0xf bank_mask:0xf
	v_mov_b32_dpp v105, v103 row_shr:8 row_mask:0xf bank_mask:0xf
	v_mov_b32_dpp v106, v100 row_shr:8 row_mask:0xf bank_mask:0xf
	v_mov_b32_dpp v107, v101 row_shr:8 row_mask:0xf bank_mask:0xf
	s_and_saveexec_b64 s[24:25], s[6:7]
	v_pk_add_f32 v[106:107], v[100:101], v[106:107]
	v_pk_add_f32 v[104:105], v[102:103], v[104:105]
	ds_write_b128 v111, v[104:107] offset:448
	s_or_b64 exec, exec, s[24:25]
	s_and_saveexec_b64 s[24:25], s[4:5]
	v_add_f32_e32 v99, v110, v99
	v_mov_b32_e32 v100, s28
	ds_write_b64 v100, v[98:99] offset:512
	s_or_b64 exec, exec, s[24:25]
	v_mov_b32_e32 v218, 0xff800000
	v_mov_b32_e32 v219, 0
	v_mov_b32_e32 v198, 0
	v_mov_b32_e32 v199, 0
	v_mov_b32_e32 v196, 0
	v_mov_b32_e32 v197, 0
	v_mov_b32_e32 v194, 0
	v_mov_b32_e32 v195, 0
	v_mov_b32_e32 v192, 0
	v_mov_b32_e32 v193, 0
	v_mov_b32_e32 v190, 0
	v_mov_b32_e32 v191, 0
	v_mov_b32_e32 v188, 0
	v_mov_b32_e32 v189, 0
	v_mov_b32_e32 v186, 0
	v_mov_b32_e32 v187, 0
	v_mov_b32_e32 v184, 0
	v_mov_b32_e32 v185, 0
	v_mov_b32_e32 v182, 0
	v_mov_b32_e32 v183, 0
	v_mov_b32_e32 v180, 0
	v_mov_b32_e32 v181, 0
	v_mov_b32_e32 v178, 0
	v_mov_b32_e32 v179, 0
	v_mov_b32_e32 v168, 0
	v_mov_b32_e32 v169, 0
	v_mov_b32_e32 v150, 0
	v_mov_b32_e32 v151, 0
	v_mov_b32_e32 v140, 0
	v_mov_b32_e32 v141, 0
	v_mov_b32_e32 v138, 0
	v_mov_b32_e32 v139, 0
	v_mov_b32_e32 v136, 0
	v_mov_b32_e32 v137, 0
	s_waitcnt lgkmcnt(0)
	s_branch .Lp1_mfma
